# speedup vs baseline: 1.0551x; 1.0052x over previous
.LBB9_1:
	s_waitcnt lgkmcnt(0)
	v_mfma_f32_32x32x16_f16 v[112:127], v[148:151], v[136:139], v[112:127]
	s_mov_b32 s14, 1
	s_mov_b64 s[34:35], 0
	s_and_b64 vcc, exec, s[30:31]
	v_mfma_f32_32x32x16_f16 v[96:111], v[144:147], v[136:139], v[96:111]
	v_mfma_f32_32x32x16_f16 v[80:95], v[140:143], v[136:139], v[80:95]
	v_mfma_f32_32x32x16_f16 v[48:63], v[128:131], v[136:139], v[48:63]
	v_mfma_f32_32x32x16_f16 v[64:79], v[148:151], v[132:135], v[64:79]
	v_mfma_f32_32x32x16_f16 v[32:47], v[144:147], v[132:135], v[32:47]
	v_mfma_f32_32x32x16_f16 v[16:31], v[140:143], v[132:135], v[16:31]
	v_mfma_f32_32x32x16_f16 v[0:15], v[128:131], v[132:135], v[0:15]
	v_mov_b32_e32 v152, v236
	v_mov_b32_e32 v153, v236
	v_mov_b32_e32 v154, v235
	v_mov_b32_e32 v155, v235
	v_mov_b32_e32 v156, v234
	v_mov_b32_e32 v157, v234
	v_mov_b32_e32 v158, v233
	v_mov_b32_e32 v159, v233
	v_pk_fma_f32 v[112:113], v[112:113], v[152:153], v[154:155]
	v_pk_fma_f32 v[114:115], v[114:115], v[152:153], v[154:155]
	v_max3_f32 v112, v112, v113, v114
	v_max3_f32 v112, v112, v115, 0
	v_cvt_f16_f32_e32 v112, v112
	ds_write_b16 v232, v112
	v_pk_fma_f32 v[116:117], v[116:117], v[152:153], v[154:155]
	v_pk_fma_f32 v[118:119], v[118:119], v[152:153], v[154:155]
	v_max3_f32 v116, v116, v117, v118
	v_max3_f32 v116, v116, v119, 0
	v_cvt_f16_f32_e32 v116, v116
	ds_write_b16 v232, v116 offset:512
	v_pk_fma_f32 v[120:121], v[120:121], v[152:153], v[154:155]
	v_pk_fma_f32 v[122:123], v[122:123], v[152:153], v[154:155]
	v_max3_f32 v120, v120, v121, v122
	v_max3_f32 v120, v120, v123, 0
	v_cvt_f16_f32_e32 v120, v120
	ds_write_b16 v232, v120 offset:1024
	v_pk_fma_f32 v[124:125], v[124:125], v[152:153], v[154:155]
	v_pk_fma_f32 v[126:127], v[126:127], v[152:153], v[154:155]
	v_max3_f32 v124, v124, v125, v126
	v_max3_f32 v124, v124, v127, 0
	v_cvt_f16_f32_e32 v124, v124
	ds_write_b16 v232, v124 offset:1536
	v_pk_fma_f32 v[96:97], v[96:97], v[152:153], v[154:155]
	v_pk_fma_f32 v[98:99], v[98:99], v[152:153], v[154:155]
	v_max3_f32 v96, v96, v97, v98
	v_max3_f32 v96, v96, v99, 0
	v_cvt_f16_f32_e32 v96, v96
	ds_write_b16 v232, v96 offset:2048
	v_pk_fma_f32 v[100:101], v[100:101], v[152:153], v[154:155]
	v_pk_fma_f32 v[102:103], v[102:103], v[152:153], v[154:155]
	v_max3_f32 v100, v100, v101, v102
	v_max3_f32 v100, v100, v103, 0
	v_cvt_f16_f32_e32 v100, v100
	ds_write_b16 v232, v100 offset:2560
	v_pk_fma_f32 v[104:105], v[104:105], v[152:153], v[154:155]
	v_pk_fma_f32 v[106:107], v[106:107], v[152:153], v[154:155]
	v_max3_f32 v104, v104, v105, v106
	v_max3_f32 v104, v104, v107, 0
	v_cvt_f16_f32_e32 v104, v104
	ds_write_b16 v232, v104 offset:3072
	v_pk_fma_f32 v[108:109], v[108:109], v[152:153], v[154:155]
	v_pk_fma_f32 v[110:111], v[110:111], v[152:153], v[154:155]
	v_max3_f32 v108, v108, v109, v110
	v_max3_f32 v108, v108, v111, 0
	v_cvt_f16_f32_e32 v108, v108
	ds_write_b16 v232, v108 offset:3584
	v_pk_fma_f32 v[80:81], v[80:81], v[152:153], v[154:155]
	v_pk_fma_f32 v[82:83], v[82:83], v[152:153], v[154:155]
	v_max3_f32 v80, v80, v81, v82
	v_max3_f32 v80, v80, v83, 0
	v_cvt_f16_f32_e32 v80, v80
	ds_write_b16 v232, v80 offset:4096
	v_pk_fma_f32 v[84:85], v[84:85], v[152:153], v[154:155]
	v_pk_fma_f32 v[86:87], v[86:87], v[152:153], v[154:155]
	v_max3_f32 v84, v84, v85, v86
	v_max3_f32 v84, v84, v87, 0
	v_cvt_f16_f32_e32 v84, v84
	ds_write_b16 v232, v84 offset:4608
	v_pk_fma_f32 v[88:89], v[88:89], v[152:153], v[154:155]
	v_pk_fma_f32 v[90:91], v[90:91], v[152:153], v[154:155]
	v_max3_f32 v88, v88, v89, v90
	v_max3_f32 v88, v88, v91, 0
	v_cvt_f16_f32_e32 v88, v88
	ds_write_b16 v232, v88 offset:5120
	v_pk_fma_f32 v[92:93], v[92:93], v[152:153], v[154:155]
	v_pk_fma_f32 v[94:95], v[94:95], v[152:153], v[154:155]
	v_max3_f32 v92, v92, v93, v94
	v_max3_f32 v92, v92, v95, 0
	v_cvt_f16_f32_e32 v92, v92
	ds_write_b16 v232, v92 offset:5632
	v_pk_fma_f32 v[48:49], v[48:49], v[152:153], v[154:155]
	v_pk_fma_f32 v[50:51], v[50:51], v[152:153], v[154:155]
	v_max3_f32 v48, v48, v49, v50
	v_max3_f32 v48, v48, v51, 0
	v_cvt_f16_f32_e32 v48, v48
	ds_write_b16 v232, v48 offset:6144
	v_pk_fma_f32 v[52:53], v[52:53], v[152:153], v[154:155]
	v_pk_fma_f32 v[54:55], v[54:55], v[152:153], v[154:155]
	v_max3_f32 v52, v52, v53, v54
	v_max3_f32 v52, v52, v55, 0
	v_cvt_f16_f32_e32 v52, v52
	ds_write_b16 v232, v52 offset:6656
	v_pk_fma_f32 v[56:57], v[56:57], v[152:153], v[154:155]
	v_pk_fma_f32 v[58:59], v[58:59], v[152:153], v[154:155]
	v_max3_f32 v56, v56, v57, v58
	v_max3_f32 v56, v56, v59, 0
	v_cvt_f16_f32_e32 v56, v56
	ds_write_b16 v232, v56 offset:7168
	v_pk_fma_f32 v[60:61], v[60:61], v[152:153], v[154:155]
	v_pk_fma_f32 v[62:63], v[62:63], v[152:153], v[154:155]
	v_max3_f32 v60, v60, v61, v62
	v_max3_f32 v60, v60, v63, 0
	v_cvt_f16_f32_e32 v60, v60
	ds_write_b16 v232, v60 offset:7680
	v_pk_fma_f32 v[64:65], v[64:65], v[156:157], v[158:159]
	v_pk_fma_f32 v[66:67], v[66:67], v[156:157], v[158:159]
	v_max3_f32 v64, v64, v65, v66
	v_max3_f32 v64, v64, v67, 0
	v_cvt_f16_f32_e32 v64, v64
	ds_write_b16 v232, v64 offset:64
	v_pk_fma_f32 v[68:69], v[68:69], v[156:157], v[158:159]
	v_pk_fma_f32 v[70:71], v[70:71], v[156:157], v[158:159]
	v_max3_f32 v68, v68, v69, v70
	v_max3_f32 v68, v68, v71, 0
	v_cvt_f16_f32_e32 v68, v68
	ds_write_b16 v232, v68 offset:576
	v_pk_fma_f32 v[72:73], v[72:73], v[156:157], v[158:159]
	v_pk_fma_f32 v[74:75], v[74:75], v[156:157], v[158:159]
	v_max3_f32 v72, v72, v73, v74
	v_max3_f32 v72, v72, v75, 0
	v_cvt_f16_f32_e32 v72, v72
	ds_write_b16 v232, v72 offset:1088
	v_pk_fma_f32 v[76:77], v[76:77], v[156:157], v[158:159]
	v_pk_fma_f32 v[78:79], v[78:79], v[156:157], v[158:159]
	v_max3_f32 v76, v76, v77, v78
	v_max3_f32 v76, v76, v79, 0
	v_cvt_f16_f32_e32 v76, v76
	ds_write_b16 v232, v76 offset:1600
	v_pk_fma_f32 v[32:33], v[32:33], v[156:157], v[158:159]
	v_pk_fma_f32 v[34:35], v[34:35], v[156:157], v[158:159]
	v_max3_f32 v32, v32, v33, v34
	v_max3_f32 v32, v32, v35, 0
	v_cvt_f16_f32_e32 v32, v32
	ds_write_b16 v232, v32 offset:2112
	v_pk_fma_f32 v[36:37], v[36:37], v[156:157], v[158:159]
	v_pk_fma_f32 v[38:39], v[38:39], v[156:157], v[158:159]
	v_max3_f32 v36, v36, v37, v38
	v_max3_f32 v36, v36, v39, 0
	v_cvt_f16_f32_e32 v36, v36
	ds_write_b16 v232, v36 offset:2624
	v_pk_fma_f32 v[40:41], v[40:41], v[156:157], v[158:159]
	v_pk_fma_f32 v[42:43], v[42:43], v[156:157], v[158:159]
	v_max3_f32 v40, v40, v41, v42
	v_max3_f32 v40, v40, v43, 0
	v_cvt_f16_f32_e32 v40, v40
	ds_write_b16 v232, v40 offset:3136
	v_pk_fma_f32 v[44:45], v[44:45], v[156:157], v[158:159]
	v_pk_fma_f32 v[46:47], v[46:47], v[156:157], v[158:159]
	v_max3_f32 v44, v44, v45, v46
	v_max3_f32 v44, v44, v47, 0
	v_cvt_f16_f32_e32 v44, v44
	ds_write_b16 v232, v44 offset:3648
	v_pk_fma_f32 v[16:17], v[16:17], v[156:157], v[158:159]
	v_pk_fma_f32 v[18:19], v[18:19], v[156:157], v[158:159]
	v_max3_f32 v16, v16, v17, v18
	v_max3_f32 v16, v16, v19, 0
	v_cvt_f16_f32_e32 v16, v16
	ds_write_b16 v232, v16 offset:4160
	v_pk_fma_f32 v[20:21], v[20:21], v[156:157], v[158:159]
	v_pk_fma_f32 v[22:23], v[22:23], v[156:157], v[158:159]
	v_max3_f32 v20, v20, v21, v22
	v_max3_f32 v20, v20, v23, 0
	v_cvt_f16_f32_e32 v20, v20
	ds_write_b16 v232, v20 offset:4672
	v_pk_fma_f32 v[24:25], v[24:25], v[156:157], v[158:159]
	v_pk_fma_f32 v[26:27], v[26:27], v[156:157], v[158:159]
	v_max3_f32 v24, v24, v25, v26
	v_max3_f32 v24, v24, v27, 0
	v_cvt_f16_f32_e32 v24, v24
	ds_write_b16 v232, v24 offset:5184
	v_pk_fma_f32 v[28:29], v[28:29], v[156:157], v[158:159]
	v_pk_fma_f32 v[30:31], v[30:31], v[156:157], v[158:159]
	v_max3_f32 v28, v28, v29, v30
	v_max3_f32 v28, v28, v31, 0
	v_cvt_f16_f32_e32 v28, v28
	ds_write_b16 v232, v28 offset:5696
	v_pk_fma_f32 v[0:1], v[0:1], v[156:157], v[158:159]
	v_pk_fma_f32 v[2:3], v[2:3], v[156:157], v[158:159]
	v_max3_f32 v0, v0, v1, v2
	v_max3_f32 v0, v0, v3, 0
	v_cvt_f16_f32_e32 v0, v0
	ds_write_b16 v232, v0 offset:6208
	v_pk_fma_f32 v[4:5], v[4:5], v[156:157], v[158:159]
	v_pk_fma_f32 v[6:7], v[6:7], v[156:157], v[158:159]
	v_max3_f32 v4, v4, v5, v6
	v_max3_f32 v4, v4, v7, 0
	v_cvt_f16_f32_e32 v4, v4
	ds_write_b16 v232, v4 offset:6720
	v_pk_fma_f32 v[8:9], v[8:9], v[156:157], v[158:159]
	v_pk_fma_f32 v[10:11], v[10:11], v[156:157], v[158:159]
	v_max3_f32 v8, v8, v9, v10
	v_max3_f32 v8, v8, v11, 0
	v_cvt_f16_f32_e32 v8, v8
	ds_write_b16 v232, v8 offset:7232
	v_pk_fma_f32 v[12:13], v[12:13], v[156:157], v[158:159]
	v_pk_fma_f32 v[14:15], v[14:15], v[156:157], v[158:159]
	v_max3_f32 v12, v12, v13, v14
	v_max3_f32 v12, v12, v15, 0
	v_cvt_f16_f32_e32 v12, v12
	ds_write_b16 v232, v12 offset:7744
	s_waitcnt vmcnt(0) lgkmcnt(0)
	s_barrier
	v_lshl_or_b32 v10, s49, 3, v224
	ds_read_b128 v[0:3], v225
	v_or_b32_e32 v4, v184, v10
	v_mov_b32_e32 v5, v185
	v_lshlrev_b64 v[4:5], 8, v[4:5]
	v_lshl_add_u64 v[8:9], v[186:187], 0, v[4:5]
	ds_read_b128 v[4:7], v226
	s_waitcnt lgkmcnt(1)
	global_store_dwordx4 v[8:9], v[0:3], off sc0 sc1
	s_nop 1
	v_or_b32_e32 v0, v188, v10
	v_mov_b32_e32 v1, v189
	v_lshlrev_b64 v[0:1], 8, v[0:1]
	v_lshl_add_u64 v[0:1], v[186:187], 0, v[0:1]
	s_waitcnt lgkmcnt(0)
	global_store_dwordx4 v[0:1], v[4:7], off sc0 sc1
	ds_read_b128 v[0:3], v227
	s_nop 0
	v_or_b32_e32 v4, v190, v10
	v_mov_b32_e32 v5, v191
	v_lshlrev_b64 v[4:5], 8, v[4:5]
	v_lshl_add_u64 v[8:9], v[186:187], 0, v[4:5]
	ds_read_b128 v[4:7], v228
	s_waitcnt lgkmcnt(1)
	global_store_dwordx4 v[8:9], v[0:3], off sc0 sc1
	s_nop 1
	v_or_b32_e32 v0, v192, v10
	v_mov_b32_e32 v1, v193
	v_lshlrev_b64 v[0:1], 8, v[0:1]
	v_lshl_add_u64 v[0:1], v[186:187], 0, v[0:1]
	s_waitcnt lgkmcnt(0)
	global_store_dwordx4 v[0:1], v[4:7], off sc0 sc1
	s_cbranch_vccnz .LBB9_31

.LBB9_31:
	s_endpgm
	s_endpgm
	s_endpgm
	s_endpgm
	s_endpgm
	s_endpgm
	s_endpgm
	s_endpgm
	s_endpgm
	s_endpgm
	s_endpgm
	s_endpgm
	s_endpgm
	s_endpgm
	s_endpgm
	s_endpgm
	s_endpgm
	s_endpgm
	s_endpgm
	s_endpgm
	s_endpgm
	s_endpgm
	s_endpgm
	s_endpgm
	s_endpgm
	s_endpgm
	s_endpgm
	s_endpgm
	s_endpgm
	s_endpgm
	s_endpgm
	s_endpgm
	s_endpgm
	.section	.rodata,"a",@progbits
	.p2align	6, 0x0
